# c23 + in IN1 the filler workgroups convert their MoE weight items before (not after) their two GEMM units, de-synchronising the epilogue store bursts
# baseline (speedup 1.0000x reference)
; __device__ __forceinline__ float row_rstd(const float* ss, int row) { const f32x4 p = *(const f32x4*)(ss + (size_t)row * 4); return 1.0f / sqrtf(((p[0] + p[1]) + (p[2] + p[3])) * (1.0f / 1024.0f) + 1e-5f); }
; #define LAS __attribute__((address_space(3)))
;     __host__ __device__ __forceinline__ bool next(int i, Unit& u) const {
;         const long L = (long)i * G + c; if (L >= nwg) return false;
;         int wgid = (int)L; { const int q = nwg / NXCD, r = nwg % NXCD, xcd = wgid % NXCD, off = wgid / NXCD; wgid = (xcd < r ? xcd * (q + 1) : r * (q + 1) + (xcd - r) * q) + off; }
;         const int nig = WGM * nN, gid = wgid / nig, fm = gid * WGM, gsz = (nM - fm) < WGM ? (nM - fm) : WGM;
;         u.pm = fm + ((wgid % nig) % gsz); u.pn = (wgid % nig) / gsz; u.ko = 0; return true;
; __global__ void __launch_bounds__(NTHREADS, 2) fwd(Args args) {
;     ...
;     if (IN(PH_IN1)) {
;         pg8::Gemm g{(const bf16*)HN8A, (const bf16*)(ws + WS_WIN1), SEQ, N_IN1, DM / 2, 0}; pg8::StaticOrder S; S.init(SEQ, N_IN1, GRID, F.bid);
;         LAS float* rtab = (LAS float*)(F.lds + MISC_OFF + 5120);
;         { pg8::Unit uu; if (S.next(0, uu) && F.tid < 256) rtab[F.tid] = pg8::row_rstd(SS1, uu.pm * 256 + F.tid) * (1.0f / 16.0f); }
.LBB0_788:
	s_cmp_lt_i32 s64, 7
	s_cselect_b64 s[4:5], -1, 0
	s_and_b64 s[10:11], s[4:5], s[8:9]
	s_andn2_b64 vcc, exec, s[10:11]
	s_cbranch_vccnz .LBB0_872
	s_mov_b32 s98, 0
	s_cmpk_lt_i32 s2, 0x80
	s_cbranch_scc1 .Lin1_gemm
	v_readlane_b32 s82, v248, 9
	s_mov_b32 s98, 2
	s_branch .Lin1_filler
.Lin1_gemm:
	s_cmpk_lt_i32 s2, 0x280
	s_cselect_b64 s[12:13], -1, 0
	s_cmpk_gt_i32 s2, 0x27f
	s_mov_b32 s3, 0
	s_cbranch_scc1 .LBB0_791
	s_ashr_i32 s0, s2, 31
	s_lshr_b32 s0, s0, 29
	s_add_i32 s0, s2, s0
	s_ashr_i32 s1, s0, 3
	s_and_b32 s0, s0, -8
	s_sub_i32 s0, s2, s0
	s_cmp_lt_i32 s0, 0
	s_movk_i32 s3, 0x51
	s_cselect_b32 s3, s3, 0x50
	s_mul_i32 s0, s0, s3
	s_add_i32 s0, s0, s1
	s_mul_hi_i32 s1, s0, 0x66666667
	s_lshr_b32 s3, s1, 31
	s_ashr_i32 s1, s1, 5
	s_add_i32 s1, s1, s3
	s_mul_i32 s3, s1, 0x50
	s_sub_i32 s0, s0, s3
	s_bfe_i32 s3, s0, 0x80000
	s_bfe_u32 s3, s3, 0x3000c
	s_add_i32 s3, s0, s3
	s_and_b32 s3, s3, 0xf8
	s_sub_i32 s0, s0, s3
	s_sext_i32_i8 s0, s0
	s_lshl_b32 s1, s1, 11
	s_lshl_b32 s0, s0, 8
	s_add_i32 s3, s1, s0

; #define LAS __attribute__((address_space(3)))
; #define DEEP_LOAD(I, v, idx) do { if ((idx) < hi) { moe_item(wg, wu, wd, wsb, (idx), I); xf8_load(I.W, I.N, I.k0, I.n0, lane, v); } } while (0)
; #define DEEP_STEP(I, v, idx) do { if ((idx) < hi) { xf8_proc(v, I.K, I.WT, I.drow0, I.k0, I.scale, scr, lane); DEEP_LOAD(I, v, (idx) + 4 * stride); } } while (0)
; __device__ __forceinline__ void moe_deep_items(const float* wg, const float* wu, const float* wd, unsigned char* wsb, int lo, int hi, int first, int stride, LAS float* scr, int lane) {
;     MoeItem I0, I1, I2, I3; f32x4 v0[8], v1[8], v2[8], v3[8];
;     int it = lo + first;
;     ...
;     DEEP_LOAD(I0, v0, it); DEEP_LOAD(I1, v1, it + stride); DEEP_LOAD(I2, v2, it + 2 * stride); DEEP_LOAD(I3, v3, it + 3 * stride);
;     for (; it < hi; it += 4 * stride) { DEEP_STEP(I0, v0, it); DEEP_STEP(I1, v1, it + stride); DEEP_STEP(I2, v2, it + 2 * stride); DEEP_STEP(I3, v3, it + 3 * stride); }
; __global__ void __launch_bounds__(NTHREADS, 2) fwd(Args args) {
;     ...
;         pg8::gemm_phase<pg8::EpiPlainBf16, pg8::StaticOrder, true, true, true>(F.lds + RING_OFF, g, S, E);
;         if (F.bid >= 128) moe_deep_items(args.in[18], args.in[19], args.in[20], ws, FILL1, FILL1 + FILL2, (F.bid - 128) * NWAVES + F.wave, 128 * NWAVES, (LAS float*)(F.lds + RING_OFF + F.wave * 16384), F.lane);
.LBB0_809:
	s_cmpk_lt_i32 s2, 0x80
	s_cbranch_scc1 .LBB0_872
	s_cmp_eq_u32 s98, 3
	s_cbranch_scc1 .LBB0_872
.Lin1_filler:
	s_add_i32 s6, s66, 0xfffffc00
	s_cmpk_lt_i32 s6, 0x1800
	s_cselect_b64 s[18:19], -1, 0
	s_cmpk_gt_i32 s6, 0x17ff
	s_cbranch_scc1 .LBB0_814
	s_mul_hi_i32 s0, s6, 0x92492493
	s_add_i32 s0, s0, s6
	s_lshr_b32 s1, s0, 31
	s_ashr_i32 s0, s0, 10
	s_add_i32 s0, s0, s1
	s_mul_hi_i32 s1, s6, 0x30c30c31
	s_lshr_b32 s3, s1, 31
	s_ashr_i32 s4, s1, 10
	s_add_i32 s4, s4, s3
	s_mul_i32 s5, s0, 0xfffff900
	s_mul_i32 s3, s4, -3
	s_add_i32 s5, s5, s6
	s_add_i32 s3, s3, s0
	s_cmp_gt_i32 s3, 1
	s_mul_hi_i32 s7, s4, 0xe00000
	s_mul_i32 s17, s4, 0xe00000
	s_cbranch_scc0 .LBB0_818
	s_lshl_b32 s0, s6, 5
	s_and_b32 s36, s0, 0x3e0
	s_add_u32 s14, s60, s17
	s_addc_u32 s15, s61, s7
	s_mul_i32 s1, s4, 0x380000
	s_mul_hi_i32 s0, s4, 0x380000
	s_add_u32 s1, s34, s1
	s_addc_u32 s0, s35, s0
	s_add_u32 s8, s1, 0x7e00000
	s_addc_u32 s9, s0, 0
	s_lshl_b32 s0, s5, 1
	s_and_b32 s37, s0, 0xffffffc0
	s_cbranch_execz .LBB0_819
	s_mov_b32 s38, 0x42000000
	s_mov_b64 s[12:13], 0x400
	s_movk_i32 s39, 0xe00
	s_mov_b32 s16, s36
	s_branch .LBB0_820

; #define LAS __attribute__((address_space(3)))
; __global__ void __launch_bounds__(NTHREADS, 2) fwd(Args args) {
;     ...
;         pg8::gemm_phase<pg8::EpiPlainBf16, pg8::StaticOrder, true, true, true>(F.lds + RING_OFF, g, S, E);
;         if (F.bid >= 128) moe_deep_items(args.in[18], args.in[19], args.in[20], ws, FILL1, FILL1 + FILL2, (F.bid - 128) * NWAVES + F.wave, 128 * NWAVES, (LAS float*)(F.lds + RING_OFF + F.wave * 16384), F.lane);
;     }
.LBB0_872:
	s_cmp_eq_u32 s98, 2
	s_cbranch_scc0 .Lin1_done
	s_mov_b32 s98, 3
	s_waitcnt lgkmcnt(0)
	s_barrier
	s_branch .Lin1_gemm
